# strategy 8 (memory issue under independent scalar work): phase A unit top requests the first sub-phase's LDS fragments and its two LDS-DMA pieces before the S.next scalar block; on top of m21
# speedup vs baseline: 1.0021x; 1.0021x over previous
; #define PG8_STAGE(bufoff, gbase, voff) do { _Pragma("unroll") for (int _i = 0; _i < 2; ++_i) \
;         __builtin_amdgcn_global_load_lds((const unsigned*)((const char*)(gbase) + (voff)[_i]), (LAS unsigned*)(lds + (bufoff) + ldsw + _i * 8192), 16, 0, 0); } while (0)
; #define PG8_WAIT_L(n) asm volatile("s_waitcnt lgkmcnt(" #n ")" ::: "memory")
; #define PG8_BAR __builtin_amdgcn_s_barrier()
; #define PG8_SCHED __builtin_amdgcn_sched_barrier(0)
;     DI bool next(int i, Unit& u) const {
;         const long L = (long)i * G + c; if (L >= nwg) return false;
;         int wgid = (int)L; { const int q = nwg / NXCD, r = nwg % NXCD, xcd = wgid % NXCD, off = wgid / NXCD; wgid = (xcd < r ? xcd * (q + 1) : r * (q + 1) + (xcd - r) * q) + off; }
;         const int nig = WGM * nN, gid = wgid / nig, fm = gid * WGM, gsz = (nM - fm) < WGM ? (nM - fm) : WGM;
;         u.pm = fm + ((wgid % nig) % gsz); u.pn = (wgid % nig) / gsz; u.e = 0; u.nv = 256; u.ui = i; return true;
; template <class Epi, class Sched, bool F8 = false>
; DI void gemm_phase(LAS unsigned char* lds, const int K, const Sched& S, const Epi& E) {
;     ...
;         const bool has_next = S.next(ui + 1, nxt);
;         const char* nA = has_next ? S.a_base(nxt) : cA; const char* nB = has_next ? S.b_base(nxt) : cB;
;         for (int t = 0; t < nt; t += 2) {
;             const bool last = (t == nt - 2); const int sxe = (t == 0) ? sx : 0;
;             const char* a1 = cA + (size_t)(t + 1) * kstep;
;             const char* a2 = last ? nA : cA + (size_t)(t + 2) * kstep; const char* b2 = last ? nB : cB + (size_t)(t + 2) * kstep;
;             const char* a3 = a2 + kstep; const char* b3 = b2 + kstep;
;             PG8_LDB(B0, 0, 0); PG8_LDB(B1, 0, 1); PG8_SCHED; PG8_LDA(At, 0, 0); PG8_STAGE(PG8_SA(1, 1), a1, oA[1]);
;             if (last && has_next) S.a_off(nxt, tid, oA);
;             PG8_WAIT_VX(sxe); PG8_WAIT_L(0); PG8_BAR; if (F8 && t == 0) { PG8_MMA0(0, 0, At, B0); PG8_MMA0(0, 1, At, B1); } else { PG8_MMA(0, 0, At, B0); PG8_MMA(0, 1, At, B1); } PG8_BAR; PG8_SCHED;
;             PG8_LDA(At, 0, 1); PG8_STAGE(PG8_SB(0, 0), b2, voffB); PG8_STAGE(PG8_SB(0, 1), b2 + hstep, voffB); PG8_STAGE(PG8_SA(0, 0), a2, oA[0]);
;             PG8_WAIT_VX(sxe); PG8_WAIT_L(0); PG8_BAR; if (F8 && t == 0) { PG8_MMA0(1, 0, At, B0); PG8_MMA0(1, 1, At, B1); } else { PG8_MMA(1, 0, At, B0); PG8_MMA(1, 1, At, B1); } PG8_BAR; PG8_SCHED;
.LBB0_273:
	v_add_u32_e32 v190, s76, v188
	v_add_u32_e32 v191, s80, v188
	ds_read_b128 v[6:9], v190
	ds_read_b128 v[10:13], v190 offset:1024
	ds_read_b128 v[14:17], v190 offset:2048
	ds_read_b128 v[18:21], v190 offset:3072
	ds_read_b128 v[22:25], v191
	ds_read_b128 v[26:29], v191 offset:1024
	ds_read_b128 v[30:33], v191 offset:2048
	ds_read_b128 v[34:37], v191 offset:3072
	v_lshl_add_u64 v[220:221], s[30:31], 0, v[170:171]
	s_add_i32 s4, s83, 0xc000
	v_lshl_add_u64 v[70:71], v[220:221], 0, s[24:25]
	s_mov_b32 m0, s4
	v_lshl_add_u64 v[226:227], s[30:31], 0, v[174:175]
	s_add_i32 s56, s83, 0xe000
	ds_read_b128 v[38:41], v189
	ds_read_b128 v[42:45], v189 offset:1024
	ds_read_b128 v[46:49], v189 offset:2048
	ds_read_b128 v[50:53], v189 offset:3072
	ds_read_b128 v[54:57], v189 offset:4096
	ds_read_b128 v[58:61], v189 offset:5120
	ds_read_b128 v[62:65], v189 offset:6144
	ds_read_b128 v[66:69], v189 offset:7168
	global_load_lds_dwordx4 v[70:71], off
	v_lshl_add_u64 v[70:71], v[226:227], 0, s[24:25]
	s_mov_b32 m0, s56
	s_nop 0
	global_load_lds_dwordx4 v[70:71], off
	s_add_i32 s96, s96, 1
	s_mul_i32 s4, s96, s38
	s_mul_hi_u32 s5, s96, s49
	s_add_i32 s5, s5, s4
	s_mul_i32 s4, s96, s49
	s_add_u32 s44, s4, s60
	s_addc_u32 s45, s5, s39
	v_mov_b64_e32 v[230:231], 0x1380
	v_cmp_lt_i64_e64 s[40:41], s[44:45], v[230:231]
	v_mov_b64_e32 v[230:231], 0x137f
	v_cmp_gt_i64_e32 vcc, s[44:45], v[230:231]
	v_mov_b64_e32 v[210:211], 0x10000
	v_mov_b64_e32 v[228:229], 0xffff
	v_mov_b32_e32 v203, 0x3727c5ac
	s_cbranch_vccnz .LBB0_275
	s_ashr_i32 s4, s44, 31
	s_lshr_b32 s4, s4, 29
	s_add_i32 s4, s44, s4
	s_ashr_i32 s5, s4, 3
	s_and_b32 s4, s4, -8
	s_sub_i32 s4, s44, s4
	s_cmp_lt_i32 s4, 0
	s_cselect_b32 s6, s2, 0x270
	s_mul_i32 s4, s4, s6
	s_add_i32 s4, s4, s5
	s_mul_hi_i32 s5, s4, 0xd20d20d3
	s_add_i32 s5, s5, s4
	s_lshr_b32 s6, s5, 31
	s_ashr_i32 s5, s5, 7
	s_add_i32 s5, s5, s6
	s_lshl_b32 s6, s5, 2
	s_sub_i32 s7, 0x80, s6
	s_min_i32 s7, s7, 4
	s_mulk_i32 s5, 0x9c
	s_sub_i32 s4, s4, s5
	s_ashr_i32 s46, s4, 2
	s_and_b32 s4, s4, 3
	s_add_i32 s42, s6, s4
.LBB0_275:
	s_ashr_i32 s43, s42, 31
	s_lshl_b64 s[4:5], s[42:43], 18
	s_add_u32 s50, s61, s4
	s_addc_u32 s51, s52, s5
	s_and_b64 s[4:5], s[40:41], exec
	s_cselect_b32 s4, s51, s31
	s_cselect_b32 s5, s50, s30
	s_ashr_i32 s47, s46, 31
	s_lshl_b64 s[6:7], s[46:47], 18
	s_add_u32 s44, s53, s6
	s_addc_u32 s45, s48, s7
	s_and_b64 s[6:7], s[40:41], exec
	s_cselect_b32 s17, s45, s67
	s_cselect_b32 s43, s44, s66
	s_add_i32 s47, s83, 0xc000
	s_waitcnt vmcnt(8)
	s_waitcnt lgkmcnt(0)
	s_barrier
	s_setprio 1
	s_waitcnt lgkmcnt(0)
	v_mfma_f32_16x16x128_f8f6f4 v[158:161], v[6:13], v[38:45], 0
	v_mfma_f32_16x16x128_f8f6f4 v[150:153], v[14:21], v[38:45], 0
	v_mfma_f32_16x16x128_f8f6f4 v[142:145], v[6:13], v[46:53], 0
	v_mfma_f32_16x16x128_f8f6f4 v[134:137], v[14:21], v[46:53], 0
	v_mfma_f32_16x16x128_f8f6f4 v[126:129], v[6:13], v[54:61], 0
	v_mfma_f32_16x16x128_f8f6f4 v[118:121], v[14:21], v[54:61], 0
	v_mfma_f32_16x16x128_f8f6f4 v[110:113], v[6:13], v[62:69], 0
	v_mfma_f32_16x16x128_f8f6f4 v[102:105], v[14:21], v[62:69], 0
	s_setprio 0
	s_setprio 1
	v_mfma_f32_16x16x128_f8f6f4 v[162:165], v[22:29], v[38:45], 0
	v_mfma_f32_16x16x128_f8f6f4 v[154:157], v[30:37], v[38:45], 0
	v_mfma_f32_16x16x128_f8f6f4 v[146:149], v[22:29], v[46:53], 0
	v_mfma_f32_16x16x128_f8f6f4 v[138:141], v[30:37], v[46:53], 0
	v_mfma_f32_16x16x128_f8f6f4 v[130:133], v[22:29], v[54:61], 0
	v_mfma_f32_16x16x128_f8f6f4 v[122:125], v[30:37], v[54:61], 0
	v_mfma_f32_16x16x128_f8f6f4 v[114:117], v[22:29], v[62:69], 0
	v_mfma_f32_16x16x128_f8f6f4 v[106:109], v[30:37], v[62:69], 0
	s_setprio 0
	s_barrier
	v_lshl_add_u64 v[180:181], s[66:67], 0, v[2:3]
	s_mov_b32 m0, s78
	v_lshl_add_u64 v[38:39], v[180:181], 0, s[28:29]
	v_lshl_add_u64 v[182:183], s[66:67], 0, v[166:167]
	s_add_u32 s6, s66, 0x20100
	ds_read_b128 v[212:215], v189 offset:16384
	ds_read_b128 v[216:219], v189 offset:17408
	ds_read_b128 v[236:239], v189 offset:18432
	ds_read_b128 v[240:243], v189 offset:19456
	ds_read_b128 v[244:247], v189 offset:20480
	ds_read_b128 v[248:251], v189 offset:21504
	ds_read_b128 v[192:195], v189 offset:22528
	ds_read_b128 v[196:199], v189 offset:23552
	global_load_lds_dwordx4 v[38:39], off
	v_lshl_add_u64 v[38:39], v[182:183], 0, s[28:29]
	s_mov_b32 m0, s79
	s_addc_u32 s7, s67, 0
	global_load_lds_dwordx4 v[38:39], off
	v_lshl_add_u64 v[38:39], s[6:7], 0, v[2:3]
	s_mov_b32 m0, s81
	v_lshl_add_u64 v[184:185], s[30:31], 0, v[168:169]
	global_load_lds_dwordx4 v[38:39], off
	v_lshl_add_u64 v[38:39], s[6:7], 0, v[166:167]
	s_mov_b32 m0, s82
	v_lshl_add_u64 v[186:187], s[30:31], 0, v[172:173]
	global_load_lds_dwordx4 v[38:39], off
	v_lshl_add_u64 v[38:39], v[184:185], 0, s[28:29]
	s_mov_b32 m0, s83
	s_nop 0
	global_load_lds_dwordx4 v[38:39], off
	v_lshl_add_u64 v[38:39], v[186:187], 0, s[28:29]
	s_mov_b32 m0, s84
	s_nop 0
	global_load_lds_dwordx4 v[38:39], off
	s_waitcnt vmcnt(8)
	s_waitcnt lgkmcnt(0)
	s_barrier
; #define PG8_STAGE(bufoff, gbase, voff) do { _Pragma("unroll") for (int _i = 0; _i < 2; ++_i) \
;         __builtin_amdgcn_global_load_lds((const unsigned*)((const char*)(gbase) + (voff)[_i]), (LAS unsigned*)(lds + (bufoff) + ldsw + _i * 8192), 16, 0, 0); } while (0)
; #define PG8_LDA(dst, b, h) do { if constexpr (F8) { _Pragma("unroll") for (int m = 0; m < 4; ++m) dst##8[m] = PG8_LD8(lds + PG8_SA(b, h) + aoff + m * 2048); } else { \
;         _Pragma("unroll") for (int m = 0; m < 4; ++m) _Pragma("unroll") for (int k = 0; k < 2; ++k) dst[m][k] = *(const LAS bf16x8*)(lds + PG8_SA(b, h) + aoff + m * 2048 + k * 1024); } } while (0)
; #define PG8_LDB(dst, b, h) do { if constexpr (F8) { _Pragma("unroll") for (int n = 0; n < 2; ++n) dst##8[n] = PG8_LD8(lds + PG8_SB(b, h) + boff + n * 2048); } else { \
;         _Pragma("unroll") for (int n = 0; n < 2; ++n) _Pragma("unroll") for (int k = 0; k < 2; ++k) dst[n][k] = *(const LAS bf16x8*)(lds + PG8_SB(b, h) + boff + n * 2048 + k * 1024); } } while (0)
; #define PG8_MMA0(ai, bj, At, Bt) do { __builtin_amdgcn_s_setprio(1); _Pragma("unroll") for (int m = 0; m < 4; ++m) _Pragma("unroll") for (int n = 0; n < 2; ++n) \
;         asm volatile("v_mfma_f32_16x16x128_f8f6f4 %0, %1, %2, 0" : "=&v"(acc[ai][bj][m][n]) : "v"(Bt##8[n]), "v"(At##8[m])); __builtin_amdgcn_s_setprio(0); } while (0)
; #define PG8_WAIT_V(n) asm volatile("s_waitcnt vmcnt(" #n ")" ::: "memory")
; #define PG8_WAIT_L(n) asm volatile("s_waitcnt lgkmcnt(" #n ")" ::: "memory")
; #define PG8_BAR __builtin_amdgcn_s_barrier()
; template <class Epi, class Sched, bool F8 = false>
; DI void gemm_phase(LAS unsigned char* lds, const int K, const Sched& S, const Epi& E) {
;     ...
;             PG8_WAIT_VX(sxe); PG8_WAIT_L(0); PG8_BAR; if (F8 && t == 0) { PG8_MMA0(1, 0, At, B0); PG8_MMA0(1, 1, At, B1); } else { PG8_MMA(1, 0, At, B0); PG8_MMA(1, 1, At, B1); } PG8_BAR; PG8_SCHED;
;             PG8_LDB(B0, 1, 0); PG8_LDB(B1, 1, 1); PG8_SCHED; PG8_LDA(At, 1, 0); PG8_STAGE(PG8_SA(0, 1), a2, oA[1]);
;             PG8_WAIT_V(8); PG8_WAIT_L(0); PG8_BAR; PG8_MMA(0, 0, At, B0); PG8_MMA(0, 1, At, B1); PG8_BAR; PG8_SCHED;
;             PG8_LDA(At, 1, 1); PG8_STAGE(PG8_SB(1, 0), b3, voffB); PG8_STAGE(PG8_SB(1, 1), b3 + hstep, voffB); PG8_STAGE(PG8_SA(1, 0), a3, oA[0]);
;             PG8_WAIT_V(8); PG8_WAIT_L(0); PG8_BAR; PG8_MMA(1, 0, At, B0); PG8_MMA(1, 1, At, B1); PG8_BAR; PG8_SCHED;
	s_setprio 1
	s_waitcnt lgkmcnt(0)
	v_mfma_f32_16x16x128_f8f6f4 v[94:97], v[6:13], v[212:219], 0
	v_mfma_f32_16x16x128_f8f6f4 v[86:89], v[14:21], v[212:219], 0
	v_mfma_f32_16x16x128_f8f6f4 v[78:81], v[6:13], v[236:243], 0
	v_mfma_f32_16x16x128_f8f6f4 v[70:73], v[14:21], v[236:243], 0
	v_mfma_f32_16x16x128_f8f6f4 v[62:65], v[6:13], v[244:251], 0
	v_mfma_f32_16x16x128_f8f6f4 v[54:57], v[14:21], v[244:251], 0
	v_mfma_f32_16x16x128_f8f6f4 v[46:49], v[6:13], v[192:199], 0
	v_mfma_f32_16x16x128_f8f6f4 v[38:41], v[14:21], v[192:199], 0
	s_setprio 0
	s_setprio 1
	v_mfma_f32_16x16x128_f8f6f4 v[98:101], v[22:29], v[212:219], 0
	v_mfma_f32_16x16x128_f8f6f4 v[90:93], v[30:37], v[212:219], 0
	v_mfma_f32_16x16x128_f8f6f4 v[82:85], v[22:29], v[236:243], 0
	v_mfma_f32_16x16x128_f8f6f4 v[74:77], v[30:37], v[236:243], 0
	v_mfma_f32_16x16x128_f8f6f4 v[66:69], v[22:29], v[244:251], 0
	v_mfma_f32_16x16x128_f8f6f4 v[58:61], v[30:37], v[244:251], 0
	v_mfma_f32_16x16x128_f8f6f4 v[50:53], v[22:29], v[192:199], 0
	v_mfma_f32_16x16x128_f8f6f4 v[42:45], v[30:37], v[192:199], 0
	s_setprio 0
	s_barrier
	v_add_u32_e32 v192, s88, v188
	v_add_u32_e32 v193, s93, v188
	ds_read_b128 v[22:25], v192
	ds_read_b128 v[26:29], v192 offset:1024
	ds_read_b128 v[30:33], v192 offset:2048
	ds_read_b128 v[34:37], v192 offset:3072
	ds_read_b128 v[6:9], v193
	ds_read_b128 v[10:13], v193 offset:1024
	ds_read_b128 v[14:17], v193 offset:2048
	ds_read_b128 v[18:21], v193 offset:3072
	s_mov_b32 m0, s85
	v_lshl_add_u64 v[220:221], v[220:221], 0, s[28:29]
	ds_read_b128 v[212:215], v189 offset:32768
	ds_read_b128 v[216:219], v189 offset:33792
	ds_read_b128 v[236:239], v189 offset:34816
	ds_read_b128 v[240:243], v189 offset:35840
	ds_read_b128 v[244:247], v189 offset:36864
	ds_read_b128 v[248:251], v189 offset:37888
	ds_read_b128 v[194:197], v189 offset:38912
	ds_read_b128 v[198:201], v189 offset:39936
	global_load_lds_dwordx4 v[220:221], off
	v_lshl_add_u64 v[220:221], v[226:227], 0, s[28:29]
	s_mov_b32 m0, s86
	s_nop 0
	global_load_lds_dwordx4 v[220:221], off
	s_waitcnt vmcnt(8)
	s_waitcnt lgkmcnt(0)
	s_barrier
	s_setprio 1
	s_waitcnt lgkmcnt(0)
	v_mfma_f32_16x16x128_f8f6f4 v[158:161], v[22:29], v[212:219], v[158:161]
	v_mfma_f32_16x16x128_f8f6f4 v[150:153], v[30:37], v[212:219], v[150:153]
	v_mfma_f32_16x16x128_f8f6f4 v[142:145], v[22:29], v[236:243], v[142:145]
	v_mfma_f32_16x16x128_f8f6f4 v[134:137], v[30:37], v[236:243], v[134:137]
	v_mfma_f32_16x16x128_f8f6f4 v[126:129], v[22:29], v[244:251], v[126:129]
	v_mfma_f32_16x16x128_f8f6f4 v[118:121], v[30:37], v[244:251], v[118:121]
	v_mfma_f32_16x16x128_f8f6f4 v[110:113], v[22:29], v[194:201], v[110:113]
	v_mfma_f32_16x16x128_f8f6f4 v[102:105], v[30:37], v[194:201], v[102:105]
	s_setprio 0
	s_setprio 1
	v_mfma_f32_16x16x128_f8f6f4 v[162:165], v[6:13], v[212:219], v[162:165]
	v_mfma_f32_16x16x128_f8f6f4 v[154:157], v[14:21], v[212:219], v[154:157]
	v_mfma_f32_16x16x128_f8f6f4 v[146:149], v[6:13], v[236:243], v[146:149]
	v_mfma_f32_16x16x128_f8f6f4 v[138:141], v[14:21], v[236:243], v[138:141]
	v_mfma_f32_16x16x128_f8f6f4 v[130:133], v[6:13], v[244:251], v[130:133]
	v_mfma_f32_16x16x128_f8f6f4 v[122:125], v[14:21], v[244:251], v[122:125]
	v_mfma_f32_16x16x128_f8f6f4 v[114:117], v[6:13], v[194:201], v[114:117]
	v_mfma_f32_16x16x128_f8f6f4 v[106:109], v[14:21], v[194:201], v[106:109]
	s_setprio 0
	s_barrier
	s_mov_b32 m0, s89
	v_lshl_add_u64 v[180:181], v[180:181], 0, s[26:27]
	s_add_u32 s6, s66, 0x20180
	ds_read_b128 v[194:197], v189 offset:49152
	ds_read_b128 v[198:201], v189 offset:50176
	ds_read_b128 v[212:215], v189 offset:51200
	ds_read_b128 v[216:219], v189 offset:52224
	ds_read_b128 v[236:239], v189 offset:53248
	ds_read_b128 v[240:243], v189 offset:54272
	ds_read_b128 v[244:247], v189 offset:55296
	ds_read_b128 v[248:251], v189 offset:56320
	global_load_lds_dwordx4 v[180:181], off
	v_lshl_add_u64 v[180:181], v[182:183], 0, s[26:27]
	s_mov_b32 m0, s90
	s_addc_u32 s7, s67, 0
	global_load_lds_dwordx4 v[180:181], off
	v_lshl_add_u64 v[180:181], s[6:7], 0, v[2:3]
	s_mov_b32 m0, s94
	s_nop 0
	global_load_lds_dwordx4 v[180:181], off
	v_lshl_add_u64 v[180:181], s[6:7], 0, v[166:167]
	s_mov_b32 m0, s95
	s_nop 0
	global_load_lds_dwordx4 v[180:181], off
	v_lshl_add_u64 v[180:181], v[184:185], 0, s[26:27]
	s_mov_b32 m0, s91
	s_nop 0
	global_load_lds_dwordx4 v[180:181], off
	v_lshl_add_u64 v[180:181], v[186:187], 0, s[26:27]
	s_mov_b32 m0, s92
	s_nop 0
	global_load_lds_dwordx4 v[180:181], off
	s_waitcnt vmcnt(8)
	s_waitcnt lgkmcnt(0)
	s_barrier
	s_setprio 1
	s_waitcnt lgkmcnt(0)
	v_mfma_f32_16x16x128_f8f6f4 v[94:97], v[22:29], v[194:201], v[94:97]
	v_mfma_f32_16x16x128_f8f6f4 v[86:89], v[30:37], v[194:201], v[86:89]
	v_mfma_f32_16x16x128_f8f6f4 v[78:81], v[22:29], v[212:219], v[78:81]
	v_mfma_f32_16x16x128_f8f6f4 v[70:73], v[30:37], v[212:219], v[70:73]
	v_mfma_f32_16x16x128_f8f6f4 v[62:65], v[22:29], v[236:243], v[62:65]
	v_mfma_f32_16x16x128_f8f6f4 v[54:57], v[30:37], v[236:243], v[54:57]
	v_mfma_f32_16x16x128_f8f6f4 v[46:49], v[22:29], v[244:251], v[46:49]
	v_mfma_f32_16x16x128_f8f6f4 v[38:41], v[30:37], v[244:251], v[38:41]
	s_setprio 0
	s_setprio 1
	v_mfma_f32_16x16x128_f8f6f4 v[98:101], v[6:13], v[194:201], v[98:101]
	v_mfma_f32_16x16x128_f8f6f4 v[90:93], v[14:21], v[194:201], v[90:93]
	v_mfma_f32_16x16x128_f8f6f4 v[82:85], v[6:13], v[212:219], v[82:85]
	v_mfma_f32_16x16x128_f8f6f4 v[74:77], v[14:21], v[212:219], v[74:77]
	v_mfma_f32_16x16x128_f8f6f4 v[66:69], v[6:13], v[236:243], v[66:69]
	v_mfma_f32_16x16x128_f8f6f4 v[58:61], v[14:21], v[236:243], v[58:61]
	v_mfma_f32_16x16x128_f8f6f4 v[50:53], v[6:13], v[244:251], v[50:53]
	v_mfma_f32_16x16x128_f8f6f4 v[42:45], v[14:21], v[244:251], v[42:45]
	s_setprio 0
	s_barrier
	s_add_u32 s6, s66, 0x200
	s_addc_u32 s7, s67, 0
	s_mov_b32 s8, 0
